# barrier-time conversion: during grid barriers 0-9 waves 1-7 of every workgroup convert one queued weight tile each (reusing the attention-phase conversion loop), layer-0 router/combine drains start la
# speedup vs baseline: 1.0173x; 1.0078x over previous
_Z3fwd6Params:
	s_mov_b32 s99, 0
	s_mov_b32 s14, s2
	s_add_u32 s2, s0, 0x118
	s_addc_u32 s3, s1, 0
	v_readfirstlane_b32 s81, v0
	v_writelane_b32 v255, s2, 0
	v_cmp_gt_u32_e32 vcc, 4, v0
	s_nop 0
	v_writelane_b32 v255, s3, 1
	s_and_saveexec_b64 s[2:3], vcc
	v_lshl_add_u32 v1, v0, 2, 0
	v_add_u32_e32 v1, 0x20000, v1
	v_mov_b32_e32 v2, 0
	ds_write_b32 v1, v2
	s_or_b64 exec, exec, s[2:3]
	s_load_dwordx2 s[34:35], s[0:1], 0x108
	s_mov_b32 s33, 0
	v_cmp_eq_u32_e32 vcc, 0, v0
	s_and_saveexec_b64 s[2:3], vcc
	s_cbranch_execz .LBB0_4
	s_load_dwordx16 s[16:31], s[0:1], 0x0
	s_add_i32 s4, 0, 0x20400
	s_load_dwordx16 s[36:51], s[0:1], 0x40
	v_mov_b32_e32 v4, s4
	s_add_i32 s4, 0, 0x20410
	s_waitcnt lgkmcnt(0)
	v_mov_b32_e32 v0, s16
	v_mov_b32_e32 v1, s17
	v_mov_b32_e32 v2, s18
	v_mov_b32_e32 v3, s19
	ds_write_b128 v4, v[0:3]
	v_mov_b32_e32 v0, s20
	v_mov_b32_e32 v1, s21
	v_mov_b32_e32 v2, s22
	v_mov_b32_e32 v3, s23
	v_mov_b32_e32 v4, s4
	s_add_i32 s4, 0, 0x20420
	ds_write_b128 v4, v[0:3]
	v_mov_b32_e32 v0, s24
	v_mov_b32_e32 v1, s25
	v_mov_b32_e32 v2, s26
	v_mov_b32_e32 v3, s27
	v_mov_b32_e32 v4, s4
	s_add_i32 s4, 0, 0x20430
	ds_write_b128 v4, v[0:3]
	v_mov_b32_e32 v0, s28
	v_mov_b32_e32 v1, s29
	v_mov_b32_e32 v2, s30
	v_mov_b32_e32 v3, s31
	v_mov_b32_e32 v4, s4
	s_add_i32 s4, 0, 0x20440
	s_load_dwordx16 s[16:31], s[0:1], 0x80
	ds_write_b128 v4, v[0:3]
	v_mov_b32_e32 v0, s36
	v_mov_b32_e32 v1, s37
	v_mov_b32_e32 v2, s38
	v_mov_b32_e32 v3, s39
	v_mov_b32_e32 v4, s4
	s_add_i32 s4, 0, 0x20450
	ds_write_b128 v4, v[0:3]
	v_mov_b32_e32 v0, s40
	v_mov_b32_e32 v1, s41
	v_mov_b32_e32 v2, s42
	v_mov_b32_e32 v3, s43
	v_mov_b32_e32 v4, s4
	s_add_i32 s4, 0, 0x20460
	ds_write_b128 v4, v[0:3]
	v_mov_b32_e32 v0, s44
	v_mov_b32_e32 v1, s45
	v_mov_b32_e32 v2, s46
	v_mov_b32_e32 v3, s47
	v_mov_b32_e32 v4, s4
	s_add_i32 s4, 0, 0x20470
	ds_write_b128 v4, v[0:3]
	v_mov_b32_e32 v0, s48
	v_mov_b32_e32 v1, s49
	v_mov_b32_e32 v2, s50
	v_mov_b32_e32 v3, s51
	v_mov_b32_e32 v4, s4
	s_add_i32 s4, 0, 0x20480
	s_load_dwordx16 s[36:51], s[0:1], 0xc0
	ds_write_b128 v4, v[0:3]
	s_waitcnt lgkmcnt(0)
	v_mov_b32_e32 v0, s16
	v_mov_b32_e32 v1, s17
	v_mov_b32_e32 v2, s18
	v_mov_b32_e32 v3, s19
	v_mov_b32_e32 v4, s4
	s_add_i32 s4, 0, 0x20490
	ds_write_b128 v4, v[0:3]
	v_mov_b32_e32 v0, s20
	v_mov_b32_e32 v1, s21
	v_mov_b32_e32 v2, s22
	v_mov_b32_e32 v3, s23
	v_mov_b32_e32 v4, s4
	s_add_i32 s4, 0, 0x204a0
	ds_write_b128 v4, v[0:3]
	v_mov_b32_e32 v0, s24
	v_mov_b32_e32 v1, s25
	v_mov_b32_e32 v2, s26
	v_mov_b32_e32 v3, s27
	v_mov_b32_e32 v4, s4
	s_add_i32 s4, 0, 0x204b0
	ds_write_b128 v4, v[0:3]
	v_mov_b32_e32 v0, s28
	v_mov_b32_e32 v1, s29
	v_mov_b32_e32 v2, s30
	v_mov_b32_e32 v3, s31
	v_mov_b32_e32 v4, s4
	s_add_i32 s4, 0, 0x204c0
	ds_write_b128 v4, v[0:3]
	v_mov_b32_e32 v0, s36
	v_mov_b32_e32 v1, s37
	v_mov_b32_e32 v2, s38
	v_mov_b32_e32 v3, s39
	v_mov_b32_e32 v4, s4
	s_add_i32 s4, 0, 0x204d0
	ds_write_b128 v4, v[0:3]
	v_mov_b32_e32 v0, s40
	v_mov_b32_e32 v1, s41
	v_mov_b32_e32 v2, s42
	v_mov_b32_e32 v3, s43
	v_mov_b32_e32 v4, s4
	s_add_i32 s4, 0, 0x204e0
	ds_write_b128 v4, v[0:3]
	v_mov_b32_e32 v4, s4
	s_load_dwordx2 s[4:5], s[0:1], 0x100
	v_mov_b32_e32 v0, s44
	v_mov_b32_e32 v1, s45
	v_mov_b32_e32 v2, s46
	v_mov_b32_e32 v3, s47
	s_add_i32 s6, 0, 0x204f0
	ds_write_b128 v4, v[0:3]
	v_mov_b32_e32 v0, s48
	v_mov_b32_e32 v1, s49
	v_mov_b32_e32 v2, s50
	v_mov_b32_e32 v3, s51
	v_mov_b32_e32 v4, s6
	s_add_i32 s6, 0, 0x20500
	ds_write_b128 v4, v[0:3]
	v_mov_b32_e32 v0, s6
	s_waitcnt lgkmcnt(0)
	v_mov_b64_e32 v[2:3], s[4:5]
	ds_write_b64 v0, v[2:3]

.LBB0_164:
	s_or_b64 exec, exec, s[0:1]
	s_cmp_lg_u32 s15, 0x100
	s_cbranch_scc1 .Lbtc_skip_0
	s_lshr_b32 s98, s81, 6
	s_cmp_eq_u32 s98, 0
	s_cbranch_scc1 .Lbtc_skip_0
	v_writelane_b32 v255, s80, 2
	v_writelane_b32 v255, s81, 3
	v_writelane_b32 v255, s82, 4
	s_mov_b32 s99, 1
	s_mul_i32 s100, s14, 7
	s_add_i32 s100, s100, s98
	s_add_i32 s100, s100, 8631
	s_mov_b32 s41, s14
	s_mov_b32 s47, s81
	s_mov_b64 s[6:7], s[34:35]
	v_mbcnt_hi_u32_b32 v184, -1, v253
	s_and_b32 s0, s81, 0xffffffc0
	v_add_u32_e32 v184, s0, v184
	s_branch .Lbtc_entry
.Lbtc_ret_0:
	s_mov_b32 s99, 0
.Lbtc_skip_0:
	s_waitcnt lgkmcnt(0)
	s_barrier

.LBB0_223:
	s_or_b64 exec, exec, s[0:1]
	s_cmp_lg_u32 s15, 0x100
	s_cbranch_scc1 .Lbtc_skip_1
	s_lshr_b32 s98, s81, 6
	s_cmp_eq_u32 s98, 0
	s_cbranch_scc1 .Lbtc_skip_1
	v_writelane_b32 v255, s80, 2
	v_writelane_b32 v255, s81, 3
	v_writelane_b32 v255, s82, 4
	s_mov_b32 s99, 2
	s_mul_i32 s100, s14, 7
	s_add_i32 s100, s100, s98
	s_add_i32 s100, s100, 10423
	s_mov_b32 s41, s14
	s_mov_b32 s47, s81
	s_mov_b64 s[6:7], s[34:35]
	v_mbcnt_hi_u32_b32 v184, -1, v253
	s_and_b32 s0, s81, 0xffffffc0
	v_add_u32_e32 v184, s0, v184
	s_branch .Lbtc_entry

.LBB0_354:
	s_or_b64 exec, exec, s[0:1]
	s_cmp_lg_u32 s15, 0x100
	s_cbranch_scc1 .Lbtc_skip_2
	s_lshr_b32 s98, s81, 6
	s_cmp_eq_u32 s98, 0
	s_cbranch_scc1 .Lbtc_skip_2
	v_writelane_b32 v255, s80, 2
	v_writelane_b32 v255, s81, 3
	v_writelane_b32 v255, s82, 4
	s_mov_b32 s99, 3
	s_mul_i32 s100, s14, 7
	s_add_i32 s100, s100, s98
	s_add_i32 s100, s100, 12215
	s_mov_b32 s41, s14
	s_mov_b32 s47, s81
	s_mov_b64 s[6:7], s[34:35]
	v_mbcnt_hi_u32_b32 v184, -1, v253
	s_and_b32 s0, s81, 0xffffffc0
	v_add_u32_e32 v184, s0, v184
	s_branch .Lbtc_entry

.LBB0_457:
	s_or_b64 exec, exec, s[0:1]
	s_cmp_lg_u32 s15, 0x100
	s_cbranch_scc1 .Lbtc_skip_3
	s_lshr_b32 s98, s81, 6
	s_cmp_eq_u32 s98, 0
	s_cbranch_scc1 .Lbtc_skip_3
	v_writelane_b32 v255, s80, 2
	v_writelane_b32 v255, s81, 3
	v_writelane_b32 v255, s82, 4
	s_mov_b32 s99, 4
	s_mul_i32 s100, s14, 7
	s_add_i32 s100, s100, s98
	s_add_i32 s100, s100, 14007
	s_mov_b32 s41, s14
	s_mov_b32 s47, s81
	s_mov_b64 s[6:7], s[34:35]
	v_mbcnt_hi_u32_b32 v184, -1, v253
	s_and_b32 s0, s81, 0xffffffc0
	v_add_u32_e32 v184, s0, v184
	s_branch .Lbtc_entry

.LBB0_543:
	s_or_b64 exec, exec, s[0:1]
	s_cmp_lg_u32 s15, 0x100
	s_cbranch_scc1 .Lbtc_skip_4
	s_lshr_b32 s98, s81, 6
	s_cmp_eq_u32 s98, 0
	s_cbranch_scc1 .Lbtc_skip_4
	v_writelane_b32 v255, s80, 2
	v_writelane_b32 v255, s81, 3
	v_writelane_b32 v255, s82, 4
	s_mov_b32 s99, 5
	s_mul_i32 s100, s14, 7
	s_add_i32 s100, s100, s98
	s_add_i32 s100, s100, 15799
	s_mov_b32 s41, s14
	s_mov_b32 s47, s81
	s_mov_b64 s[6:7], s[34:35]
	v_mbcnt_hi_u32_b32 v184, -1, v253
	s_and_b32 s0, s81, 0xffffffc0
	v_add_u32_e32 v184, s0, v184
	s_branch .Lbtc_entry

.Lbtc_entry:
	s_ashr_i32 s0, s47, 6
	s_lshl_b32 s1, s41, 3
	s_add_i32 s40, s1, s0
	s_add_u32 s41, s6, 0x17458000
	s_mulk_i32 s0, 0x2400
	s_addc_u32 s43, s7, 0
	s_add_i32 s0, s0, 0
	s_add_u32 s44, s6, 0x7458000
	s_addc_u32 s45, s7, 0
	s_add_u32 s47, s6, 0x6458000
	s_addc_u32 s48, s7, 0
	s_add_u32 s49, s6, 0x5458000
	s_addc_u32 s50, s7, 0
	s_add_u32 s51, s6, 0x4d58000
	s_addc_u32 s52, s7, 0
	s_add_u32 s53, s6, 0x158000
	s_addc_u32 s54, s7, 0
	s_add_u32 s55, s6, 0x3390c000
	v_lshlrev_b32_e32 v2, 4, v184
	s_addc_u32 s56, s7, 0
	v_lshlrev_b32_e32 v0, 2, v184
	v_and_b32_e32 v78, 48, v2
	s_add_u32 s57, s6, 0x35e0c000
	v_lshlrev_b32_e32 v2, 1, v184
	v_and_b32_e32 v82, 48, v184
	v_and_b32_e32 v0, 60, v0
	v_bfe_u32 v83, v184, 2, 4
	s_addc_u32 s58, s7, 0
	v_and_b32_e32 v2, 0x60, v2
	v_and_b32_e32 v8, 7, v184
	v_bfe_u32 v87, v184, 3, 3
	v_mov_b32_e32 v77, 0
	v_add_u32_e32 v1, s0, v82
	v_mul_u32_u24_e32 v3, 0x50, v0
	v_add_u32_e32 v4, s0, v78
	v_mul_u32_u24_e32 v5, 0x50, v83
	s_add_u32 s59, s6, 0x3760c000
	v_add_u32_e32 v6, s0, v2
	v_mul_u32_u24_e32 v7, 0x90, v0
	v_lshlrev_b32_e32 v2, 3, v8
	v_lshl_add_u32 v8, v8, 4, s0
	v_mul_u32_u24_e32 v9, 0x90, v87
	s_mul_i32 s40, s40, 9
	s_mov_b32 s1, 0
	v_mov_b32_e32 v79, v77
	v_or_b32_e32 v84, 16, v83
	v_or_b32_e32 v85, 32, v83
	v_or_b32_e32 v86, 48, v83
	s_addc_u32 s60, s7, 0
	v_or_b32_e32 v88, 8, v87
	v_or_b32_e32 v89, 16, v87
	v_or_b32_e32 v90, 24, v87
	v_or_b32_e32 v91, 32, v87
	v_or_b32_e32 v92, 40, v87
	v_or_b32_e32 v93, 48, v87
	v_or_b32_e32 v94, 56, v87
	s_mov_b32 s65, -9
	s_cmp_eq_u32 s99, 0
	s_cbranch_scc1 .Lbtc_normal
	s_mov_b32 s40, s100
	s_mov_b32 s65, -1
.Lbtc_normal:
	s_add_i32 s61, 0, 0x204f8
	s_movk_i32 s62, 0x2000
	s_movk_i32 s63, 0x4000
	s_movk_i32 s64, 0x6000
	s_mov_b32 s66, 0x12000
	s_mov_b32 s67, 0xc3e00000
	v_add_u32_e32 v95, v1, v3
	v_add_u32_e32 v96, v4, v5
	s_movk_i32 s68, 0x3000
	s_movk_i32 s69, 0x5000
	s_movk_i32 s70, 0x7000
	s_add_i32 s71, 0, 0x204c0
	s_add_i32 s72, 0, 0x204b8
	s_add_i32 s73, 0, 0x204b0
	s_add_i32 s74, 0, 0x204a8
	s_add_i32 s75, 0, 0x20458
	s_add_i32 s76, 0, 0x20448
	s_add_i32 s77, 0, 0x20440
	s_mov_b32 s78, 0x9000
	s_mov_b32 s79, 0x1b000
	s_mov_b32 s80, 0x25000
	s_mov_b32 s81, 0x2e000
	s_mov_b32 s82, 0x37000
	s_mov_b32 s83, 0x41000
	s_mov_b32 s84, 0x4a000
	s_mov_b32 s85, 0x53000
	s_mov_b32 s86, 0x5d000
	s_mov_b32 s87, 0x66000
	s_mov_b32 s88, 0x6f000
	s_mov_b32 s89, 0x79000
	s_mov_b32 s90, 0x82000
	s_mov_b32 s91, 0x8b000
	v_add_u32_e32 v97, v6, v7
	v_lshlrev_b32_e32 v76, 1, v2
	v_lshlrev_b32_e32 v80, 2, v0
	v_mov_b32_e32 v98, 0x43e00000
	v_mov_b32_e32 v100, v77
	v_mov_b32_e32 v101, v77
	v_mov_b32_e32 v102, v77
	v_mov_b32_e32 v103, v77
	v_add_u32_e32 v99, v8, v9
	s_branch .LBB0_647

.LBB0_719:
	s_mov_b64 s[0:1], 0
	v_readlane_b32 s80, v255, 2
	v_readlane_b32 s81, v255, 3
	v_readlane_b32 s82, v255, 4
	s_cmp_eq_u32 s99, 0
	s_cbranch_scc1 .Lbtc_none
	s_cmp_eq_u32 s99, 1
	s_cbranch_scc1 .Lbtc_ret_0
	s_cmp_eq_u32 s99, 2
	s_cbranch_scc1 .Lbtc_ret_1
	s_cmp_eq_u32 s99, 3
	s_cbranch_scc1 .Lbtc_ret_2
	s_cmp_eq_u32 s99, 4
	s_cbranch_scc1 .Lbtc_ret_3
	s_cmp_eq_u32 s99, 5
	s_cbranch_scc1 .Lbtc_ret_4
	s_cmp_eq_u32 s99, 6
	s_cbranch_scc1 .Lbtc_ret_5
	s_cmp_eq_u32 s99, 7
	s_cbranch_scc1 .Lbtc_ret_6
	s_cmp_eq_u32 s99, 8
	s_cbranch_scc1 .Lbtc_ret_7
	s_cmp_eq_u32 s99, 9
	s_cbranch_scc1 .Lbtc_ret_8
	s_cmp_eq_u32 s99, 10
	s_cbranch_scc1 .Lbtc_ret_9
.Lbtc_none:
.LBB0_720:
	s_and_b64 vcc, exec, s[0:1]
	s_cbranch_vccz .LBB0_845
	s_add_u32 s21, s6, 0x3c01c800
	s_addc_u32 s25, s7, 0
	v_max_i32_e32 v0, 0xffffffd1, v184
	s_add_u32 s43, s6, 0x3c01cc00
	v_sub_u32_e32 v0, v0, v184
	s_addc_u32 s44, s7, 0
	v_add_u32_e32 v0, 0x1ff, v0
	s_add_u32 s45, s6, 0x3c01d000
	v_lshrrev_b32_e32 v1, 9, v0
	s_addc_u32 s47, s7, 0
	v_add_u32_e32 v2, 1, v1
	v_add_u32_e32 v1, -1, v1
	s_add_u32 s48, s6, 0x216b8800
	s_movk_i32 s2, 0x1ff
	v_lshrrev_b32_e32 v3, 1, v1
	s_addc_u32 s49, s7, 0
	v_add_u32_e32 v3, 1, v3
	v_cmp_lt_u32_e64 s[2:3], s2, v0
	v_and_b32_e32 v0, 0xfffffe, v2
	s_movk_i32 s0, 0x1d1
	s_add_u32 s50, s6, 0x216b8400
	v_lshl_add_u32 v173, v0, 9, v184
	v_and_b32_e32 v174, 3, v3
	v_cmp_ne_u32_e64 s[8:9], v2, v0
	v_add_u32_e32 v0, 0, v172
	v_cmp_gt_i32_e64 s[0:1], s0, v184
	s_addc_u32 s51, s7, 0
	v_add_u32_e32 v185, 0x200, v184
	v_cmp_lt_u32_e64 s[4:5], 5, v1
	v_and_b32_e32 v175, -4, v3
	v_cmp_ne_u32_e64 s[6:7], 0, v174
	v_add_u32_e32 v176, 0x18800, v0
	v_add_u32_e32 v177, 0x19000, v0
	s_movk_i32 s52, 0x80
	s_movk_i32 s53, 0x70
	s_movk_i32 s18, 0x800
	s_mov_b32 s20, 0x3fb8aa3b
	s_mov_b64 s[22:23], 0x800
	s_movk_i32 s54, 0xffd0
	s_add_i32 s55, 0, 0x20478
	s_movk_i32 s56, 0x4c00
	v_mov_b32_e32 v163, 0
	v_mov_b32_e32 v178, 0x358637bd
	s_mov_b32 s57, 0x800000
	s_add_i32 s58, 0, 0x10000
	s_movk_i32 s59, 0xc0
	s_movk_i32 s60, 0x60
	s_movk_i32 s61, 0xa0
	s_movk_i32 s62, 0xe0
	s_mov_b32 s24, 0x3e0293ee
	s_mov_b32 s63, 0x4138aa3b
	s_mov_b32 s64, 0xc3e00000
	v_mov_b32_e32 v179, 0x43e00000
	s_branch .LBB0_723

.LBB0_894:
	s_or_b64 exec, exec, s[0:1]
	s_cmp_lg_u32 s15, 0x100
	s_cbranch_scc1 .Lbtc_skip_5
	s_lshr_b32 s98, s81, 6
	s_cmp_eq_u32 s98, 0
	s_cbranch_scc1 .Lbtc_skip_5
	v_writelane_b32 v255, s80, 2
	v_writelane_b32 v255, s81, 3
	v_writelane_b32 v255, s82, 4
	s_mov_b32 s99, 6
	s_mul_i32 s100, s14, 7
	s_add_i32 s100, s100, s98
	s_add_i32 s100, s100, 17591
	s_mov_b32 s41, s14
	s_mov_b32 s47, s81
	s_mov_b64 s[6:7], s[34:35]
	v_mbcnt_hi_u32_b32 v184, -1, v253
	s_and_b32 s0, s81, 0xffffffc0
	v_add_u32_e32 v184, s0, v184
	s_branch .Lbtc_entry

.LBB0_968:
	s_or_b64 exec, exec, s[0:1]
	s_cmp_lg_u32 s15, 0x100
	s_cbranch_scc1 .Lbtc_skip_6
	s_lshr_b32 s98, s81, 6
	s_cmp_eq_u32 s98, 0
	s_cbranch_scc1 .Lbtc_skip_6
	v_writelane_b32 v255, s80, 2
	v_writelane_b32 v255, s81, 3
	v_writelane_b32 v255, s82, 4
	s_mov_b32 s99, 7
	s_mul_i32 s100, s14, 7
	s_add_i32 s100, s100, s98
	s_add_i32 s100, s100, 19383
	s_mov_b32 s41, s14
	s_mov_b32 s47, s81
	s_mov_b64 s[6:7], s[34:35]
	v_mbcnt_hi_u32_b32 v184, -1, v253
	s_and_b32 s0, s81, 0xffffffc0
	v_add_u32_e32 v184, s0, v184
	s_branch .Lbtc_entry

.LBB0_1042:
	s_or_b64 exec, exec, s[0:1]
	s_cmp_lg_u32 s15, 0x100
	s_cbranch_scc1 .Lbtc_skip_7
	s_lshr_b32 s98, s81, 6
	s_cmp_eq_u32 s98, 0
	s_cbranch_scc1 .Lbtc_skip_7
	v_writelane_b32 v255, s80, 2
	v_writelane_b32 v255, s81, 3
	v_writelane_b32 v255, s82, 4
	s_mov_b32 s99, 8
	s_mul_i32 s100, s14, 7
	s_add_i32 s100, s100, s98
	s_add_i32 s100, s100, 21175
	s_mov_b32 s41, s14
	s_mov_b32 s47, s81
	s_mov_b64 s[6:7], s[34:35]
	v_mbcnt_hi_u32_b32 v184, -1, v253
	s_and_b32 s0, s81, 0xffffffc0
	v_add_u32_e32 v184, s0, v184
	s_branch .Lbtc_entry

.LBB0_1058:
	s_add_i32 s1, s40, 0xffffff78
	s_lshl_b32 s0, s38, 3
	s_max_i32 s1, s1, 0
	s_mulk_i32 s1, 0x48
	s_cmp_eq_u32 s40, 0x100
	s_cselect_b32 s98, 14336, 0
	s_add_i32 s1, s1, s98
	s_add_i32 s0, s42, s0
	s_add_i32 s43, s0, s1
	s_cmpk_gt_i32 s43, 0x5fff
	s_mov_b32 s1, 0
	s_cbranch_scc1 .LBB0_1135
	s_lshl_b32 s44, s40, 3
	s_add_u32 s45, s10, 0x17458000
	s_mul_i32 s0, s42, 0x2400
	s_addc_u32 s46, s11, 0
	s_add_i32 s0, s0, 0
	s_add_u32 s47, s10, 0x7458000
	s_addc_u32 s48, s11, 0
	s_add_u32 s49, s10, 0x6458000
	s_addc_u32 s50, s11, 0
	s_add_u32 s51, s10, 0x5458000
	s_addc_u32 s52, s11, 0
	s_add_u32 s53, s10, 0x4d58000
	s_addc_u32 s54, s11, 0
	s_add_u32 s55, s10, 0x158000
	s_addc_u32 s56, s11, 0
	s_add_u32 s57, s10, 0x3390c000
	s_addc_u32 s58, s11, 0
	s_add_u32 s59, s10, 0x35e0c000
	v_lshlrev_b32_e32 v2, 1, v86
	v_and_b32_e32 v0, 60, v0
	v_and_b32_e32 v80, 48, v54
	s_addc_u32 s60, s11, 0
	v_and_b32_e32 v2, 0x60, v2
	v_and_b32_e32 v8, 7, v85
	v_lshrrev_b32_e32 v90, 3, v86
	v_mov_b32_e32 v79, 0
	v_add_u32_e32 v1, s0, v76
	v_mul_u32_u24_e32 v3, 0x50, v0
	v_add_u32_e32 v4, s0, v80
	v_mul_u32_u24_e32 v5, 0x50, v87
	s_add_u32 s61, s10, 0x3760c000
	v_add_u32_e32 v6, s0, v2
	v_mul_u32_u24_e32 v7, 0x90, v0
	v_lshlrev_b32_e32 v2, 3, v8
	v_lshl_add_u32 v8, v8, 4, s0
	v_mul_u32_u24_e32 v9, 0x90, v90
	v_mov_b32_e32 v81, v79
	v_or_b32_e32 v77, 16, v87
	v_or_b32_e32 v88, 32, v87
	v_or_b32_e32 v89, 48, v87
	s_addc_u32 s62, s11, 0
	v_or_b32_e32 v91, 8, v90
	v_or_b32_e32 v92, 16, v90
	v_or_b32_e32 v93, 24, v90
	v_or_b32_e32 v94, 32, v90
	v_or_b32_e32 v95, 40, v90
	v_or_b32_e32 v96, 48, v90
	v_or_b32_e32 v97, 56, v90
	s_add_i32 s63, 0, 0x204f8
	s_movk_i32 s64, 0x2000
	s_movk_i32 s65, 0x4000
	s_movk_i32 s66, 0x6000
	s_mov_b32 s67, 0x12000
	s_mov_b32 s68, 0xc3e00000
	v_add_u32_e32 v98, v1, v3
	v_add_u32_e32 v99, v4, v5
	s_movk_i32 s69, 0x3000
	s_movk_i32 s70, 0x5000
	s_movk_i32 s71, 0x7000
	s_add_i32 s72, 0, 0x204c0
	s_add_i32 s73, 0, 0x204b8
	s_add_i32 s74, 0, 0x204b0
	s_add_i32 s75, 0, 0x204a8
	s_add_i32 s76, 0, 0x20458
	s_add_i32 s77, 0, 0x20448
	s_add_i32 s78, 0, 0x20440
	s_mov_b32 s79, 0x9000
	s_mov_b32 s80, 0x1b000
	s_mov_b32 s81, 0x25000
	s_mov_b32 s82, 0x2e000
	s_mov_b32 s83, 0x37000
	s_mov_b32 s84, 0x41000
	s_mov_b32 s85, 0x4a000
	s_mov_b32 s86, 0x53000
	s_mov_b32 s87, 0x5d000
	s_mov_b32 s88, 0x66000
	s_mov_b32 s89, 0x6f000
	s_mov_b32 s90, 0x79000
	s_mov_b32 s91, 0x82000
	s_mov_b32 s92, 0x8b000
	v_add_u32_e32 v100, v6, v7
	v_lshlrev_b32_e32 v78, 1, v2
	v_lshlrev_b32_e32 v82, 2, v0
	v_mov_b32_e32 v101, 0x43e00000
	v_mov_b32_e32 v104, v79
	v_mov_b32_e32 v105, v79
	v_mov_b32_e32 v106, v79
	v_mov_b32_e32 v107, v79
	v_add_u32_e32 v102, v8, v9
	s_branch .LBB0_1062

.LBB0_1197:
	s_or_b64 exec, exec, s[0:1]
	s_cmp_lg_u32 s15, 0x100
	s_cbranch_scc1 .Lbtc_skip_8
	s_lshr_b32 s98, s81, 6
	s_cmp_eq_u32 s98, 0
	s_cbranch_scc1 .Lbtc_skip_8
	v_writelane_b32 v255, s80, 2
	v_writelane_b32 v255, s81, 3
	v_writelane_b32 v255, s82, 4
	s_mov_b32 s99, 9
	s_mul_i32 s100, s14, 7
	s_add_i32 s100, s100, s98
	s_add_i32 s100, s100, 24567
	s_mov_b32 s41, s14
	s_mov_b32 s47, s81
	s_mov_b64 s[6:7], s[34:35]
	v_mbcnt_hi_u32_b32 v184, -1, v253
	s_and_b32 s0, s81, 0xffffffc0
	v_add_u32_e32 v184, s0, v184
	s_branch .Lbtc_entry

.LBB0_1341:
	s_or_b64 exec, exec, s[0:1]
	s_cmp_lg_u32 s15, 0x100
	s_cbranch_scc1 .Lbtc_skip_9
	s_lshr_b32 s98, s81, 6
	s_cmp_eq_u32 s98, 0
	s_cbranch_scc1 .Lbtc_skip_9
	v_writelane_b32 v255, s80, 2
	v_writelane_b32 v255, s81, 3
	v_writelane_b32 v255, s82, 4
	s_mov_b32 s99, 10
	s_mul_i32 s100, s14, 7
	s_add_i32 s100, s100, s98
	s_add_i32 s100, s100, 26359
	s_mov_b32 s41, s14
	s_mov_b32 s47, s81
	s_mov_b64 s[6:7], s[34:35]
	v_mbcnt_hi_u32_b32 v184, -1, v253
	s_and_b32 s0, s81, 0xffffffc0
	v_add_u32_e32 v184, s0, v184
	s_branch .Lbtc_entry

.LBB0_1412:
	s_cmpk_lt_i32 s4, 0x1cc0
	s_barrier
	s_cbranch_scc0 .LBB0_1489
	s_add_u32 s3, s0, 0x17458000
	s_mulk_i32 s12, 0x2400
	s_addc_u32 s40, s1, 0
	s_add_i32 s6, s12, 0
	s_add_u32 s41, s0, 0x7458000
	s_addc_u32 s42, s1, 0
	s_add_u32 s43, s0, 0x6458000
	s_addc_u32 s44, s1, 0
	s_add_u32 s45, s0, 0x5458000
	s_addc_u32 s46, s1, 0
	s_add_u32 s47, s0, 0x4d58000
	s_addc_u32 s48, s1, 0
	s_add_u32 s49, s0, 0x158000
	s_addc_u32 s50, s1, 0
	s_add_u32 s51, s0, 0x3390c000
	s_addc_u32 s52, s1, 0
	s_add_u32 s53, s0, 0x35e0c000
	v_lshlrev_b32_e32 v7, 1, v1
	v_and_b32_e32 v75, 48, v0
	v_and_b32_e32 v2, 60, v2
	v_and_b32_e32 v70, 48, v3
	v_lshrrev_b32_e32 v76, 2, v1
	s_addc_u32 s54, s1, 0
	v_and_b32_e32 v7, 0x60, v7
	v_and_b32_e32 v9, 7, v0
	v_lshrrev_b32_e32 v80, 3, v1
	v_mov_b32_e32 v69, 0
	v_add_u32_e32 v4, s6, v75
	v_mul_u32_u24_e32 v5, 0x50, v2
	v_add_u32_e32 v3, s6, v70
	v_mul_u32_u24_e32 v6, 0x50, v76
	s_add_u32 s55, s0, 0x3760c000
	v_add_u32_e32 v7, s6, v7
	v_mul_u32_u24_e32 v8, 0x90, v2
	v_lshlrev_b32_e32 v0, 3, v9
	v_lshl_add_u32 v9, v9, 4, s6
	v_mul_u32_u24_e32 v1, 0x90, v80
	s_mov_b32 s5, 0
	v_mov_b32_e32 v71, v69
	v_or_b32_e32 v77, 16, v76
	v_or_b32_e32 v78, 32, v76
	v_or_b32_e32 v79, 48, v76
	s_addc_u32 s56, s1, 0
	v_or_b32_e32 v81, 8, v80
	v_or_b32_e32 v82, 16, v80
	v_or_b32_e32 v83, 24, v80
	v_or_b32_e32 v84, 32, v80
	v_or_b32_e32 v85, 40, v80
	v_or_b32_e32 v86, 48, v80
	v_or_b32_e32 v87, 56, v80
	s_add_i32 s57, s4, 0xf97f
	s_cmp_eq_u32 s15, 0x100
	s_cselect_b32 s98, 3584, 0
	s_add_i32 s57, s57, s98
	s_add_i32 s58, 0, 0x204f8
	s_movk_i32 s59, 0x2000
	s_movk_i32 s60, 0x4000
	s_movk_i32 s61, 0x6000
	s_mov_b32 s62, 0x12000
	s_mov_b32 s63, 0x18000
	s_mov_b32 s64, 0x1a000
	s_mov_b32 s65, 0x1c000
	s_mov_b32 s66, 0x1e000
	s_mov_b32 s67, 0xc3e00000
	v_add_u32_e32 v88, v4, v5
	v_add_u32_e32 v89, v3, v6
	s_movk_i32 s68, 0x1000
	s_movk_i32 s69, 0x3000
	s_movk_i32 s70, 0x5000
	s_movk_i32 s71, 0x7000
	s_add_i32 s72, 0, 0x204c0
	s_add_i32 s73, 0, 0x204b8
	s_add_i32 s74, 0, 0x204b0
	s_add_i32 s75, 0, 0x204a8
	s_add_i32 s76, 0, 0x20458
	s_add_i32 s77, 0, 0x20448
	s_add_i32 s78, 0, 0x20440
	s_mov_b32 s79, 0x9000
	s_mov_b32 s80, 0x1b000
	s_mov_b32 s81, 0x25000
	s_mov_b32 s82, 0x2e000
	s_mov_b32 s83, 0x37000
	s_mov_b32 s84, 0x41000
	s_mov_b32 s85, 0x4a000
	s_mov_b32 s86, 0x53000
	s_mov_b32 s87, 0x5d000
	s_mov_b32 s88, 0x66000
	s_mov_b32 s89, 0x6f000
	s_mov_b32 s90, 0x79000
	s_mov_b32 s91, 0x82000
	s_mov_b32 s92, 0x8b000
	v_add_u32_e32 v90, v7, v8
	v_lshlrev_b32_e32 v68, 1, v0
	v_lshlrev_b32_e32 v72, 2, v2
	v_mov_b32_e32 v91, 0x43e00000
	v_mov_b32_e32 v94, v69
	v_mov_b32_e32 v95, v69
	v_mov_b32_e32 v96, v69
	v_mov_b32_e32 v97, v69
	v_add_u32_e32 v92, v9, v1
	s_branch .LBB0_1416

	.amdhsa_kernel _Z3fwd6Params
		.amdhsa_group_segment_fixed_size 0
		.amdhsa_private_segment_fixed_size 0
		.amdhsa_kernarg_size 536
		.amdhsa_user_sgpr_count 2
		.amdhsa_user_sgpr_dispatch_ptr 0
		.amdhsa_user_sgpr_queue_ptr 0
		.amdhsa_user_sgpr_kernarg_segment_ptr 1
		.amdhsa_user_sgpr_dispatch_id 0
		.amdhsa_user_sgpr_kernarg_preload_length 0
		.amdhsa_user_sgpr_kernarg_preload_offset 0
		.amdhsa_user_sgpr_private_segment_size 0
		.amdhsa_uses_dynamic_stack 0
		.amdhsa_enable_private_segment 0
		.amdhsa_system_sgpr_workgroup_id_x 1
		.amdhsa_system_sgpr_workgroup_id_y 0
		.amdhsa_system_sgpr_workgroup_id_z 0
		.amdhsa_system_sgpr_workgroup_info 0
		.amdhsa_system_vgpr_workitem_id 0
		.amdhsa_next_free_vgpr 256
		.amdhsa_next_free_sgpr 101
		.amdhsa_accum_offset 256
		.amdhsa_reserve_vcc 1
		.amdhsa_float_round_mode_32 0
		.amdhsa_float_round_mode_16_64 0
		.amdhsa_float_denorm_mode_32 3
		.amdhsa_float_denorm_mode_16_64 3
		.amdhsa_dx10_clamp 1
		.amdhsa_ieee_mode 1
		.amdhsa_fp16_overflow 0
		.amdhsa_tg_split 0
		.amdhsa_exception_fp_ieee_invalid_op 0
		.amdhsa_exception_fp_denorm_src 0
		.amdhsa_exception_fp_ieee_div_zero 0
		.amdhsa_exception_fp_ieee_overflow 0
		.amdhsa_exception_fp_ieee_underflow 0
		.amdhsa_exception_fp_ieee_inexact 0
		.amdhsa_exception_int_div_zero 0
	.end_amdhsa_kernel

amdhsa.kernels:
  - .agpr_count:     0
    .args:
      - .offset:         0
        .size:           280
        .value_kind:     by_value
      - .offset:         280
        .size:           4
        .value_kind:     hidden_block_count_x
      - .offset:         284
        .size:           4
        .value_kind:     hidden_block_count_y
      - .offset:         288
        .size:           4
        .value_kind:     hidden_block_count_z
      - .offset:         292
        .size:           2
        .value_kind:     hidden_group_size_x
      - .offset:         294
        .size:           2
        .value_kind:     hidden_group_size_y
      - .offset:         296
        .size:           2
        .value_kind:     hidden_group_size_z
      - .offset:         298
        .size:           2
        .value_kind:     hidden_remainder_x
      - .offset:         300
        .size:           2
        .value_kind:     hidden_remainder_y
      - .offset:         302
        .size:           2
        .value_kind:     hidden_remainder_z
      - .offset:         320
        .size:           8
        .value_kind:     hidden_global_offset_x
      - .offset:         328
        .size:           8
        .value_kind:     hidden_global_offset_y
      - .offset:         336
        .size:           8
        .value_kind:     hidden_global_offset_z
      - .offset:         344
        .size:           2
        .value_kind:     hidden_grid_dims
      - .offset:         400
        .size:           4
        .value_kind:     hidden_dynamic_lds_size
    .group_segment_fixed_size: 0
    .kernarg_segment_align: 8
    .kernarg_segment_size: 536
    .language:       OpenCL C
    .language_version:
      - 2
      - 0
    .max_flat_workgroup_size: 512
    .name:           _Z3fwd6Params
    .private_segment_fixed_size: 0
    .sgpr_count:     107
    .sgpr_spill_count: 5
    .symbol:         _Z3fwd6Params.kd
    .uniform_work_group_size: 1
    .uses_dynamic_stack: false
    .vgpr_count:     256
    .vgpr_spill_count: 0
    .wavefront_size: 64
